# previous best with the eight GEMM K-loop head labels aligned to 64 bytes (p2align 6)
# speedup vs baseline: 1.0029x; 1.0028x over previous
.LBB0_287:
	s_andn2_b64 vcc, exec, s[48:49]
	s_cbranch_vccnz .LBB0_297
	s_add_u32 s1, s10, 0x100
	s_addc_u32 s68, s11, 0
	s_add_u32 s69, s12, 0x100
	s_addc_u32 s70, s13, 0
	s_add_u32 s71, s8, 0x100
	s_addc_u32 s72, s9, 0
	s_add_u32 s73, s14, 0x100
	v_mov_b32_e32 v0, 0
	s_addc_u32 vcc_lo, s15, 0
	s_mov_b32 s8, 0
	v_mov_b32_e32 v1, v0
	v_mov_b32_e32 v2, v0
	v_mov_b32_e32 v3, v0
	v_mov_b32_e32 v4, v0
	v_mov_b32_e32 v5, v0
	v_mov_b32_e32 v6, v0
	v_mov_b32_e32 v7, v0
	v_mov_b32_e32 v16, v0
	v_mov_b32_e32 v17, v0
	v_mov_b32_e32 v18, v0
	v_mov_b32_e32 v19, v0
	s_waitcnt vmcnt(0)
	v_mov_b32_e32 v20, v0
	v_mov_b32_e32 v21, v0
	v_mov_b32_e32 v22, v0
	v_mov_b32_e32 v23, v0
	v_mov_b32_e32 v32, v0
	v_mov_b32_e32 v33, v0
	v_mov_b32_e32 v34, v0
	v_mov_b32_e32 v35, v0
	v_mov_b32_e32 v36, v0
	v_mov_b32_e32 v37, v0
	v_mov_b32_e32 v38, v0
	v_mov_b32_e32 v39, v0
	v_mov_b32_e32 v48, v0
	v_mov_b32_e32 v49, v0
	v_mov_b32_e32 v50, v0
	v_mov_b32_e32 v51, v0
	v_mov_b32_e32 v52, v0
	v_mov_b32_e32 v53, v0
	v_mov_b32_e32 v54, v0
	v_mov_b32_e32 v55, v0
	v_mov_b32_e32 v8, v0
	v_mov_b32_e32 v9, v0
	v_mov_b32_e32 v10, v0
	v_mov_b32_e32 v11, v0
	v_mov_b32_e32 v12, v0
	v_mov_b32_e32 v13, v0
	v_mov_b32_e32 v14, v0
	v_mov_b32_e32 v15, v0
	v_mov_b32_e32 v24, v0
	v_mov_b32_e32 v25, v0
	v_mov_b32_e32 v26, v0
	v_mov_b32_e32 v27, v0
	v_mov_b32_e32 v28, v0
	v_mov_b32_e32 v29, v0
	v_mov_b32_e32 v30, v0
	v_mov_b32_e32 v31, v0
	v_mov_b32_e32 v40, v0
	v_mov_b32_e32 v41, v0
	v_mov_b32_e32 v42, v0
	v_mov_b32_e32 v43, v0
	v_mov_b32_e32 v44, v0
	v_mov_b32_e32 v45, v0
	v_mov_b32_e32 v46, v0
	v_mov_b32_e32 v47, v0
	v_mov_b32_e32 v56, v0
	v_mov_b32_e32 v57, v0
	v_mov_b32_e32 v58, v0
	v_mov_b32_e32 v59, v0
	v_mov_b32_e32 v60, v0
	v_mov_b32_e32 v61, v0
	v_mov_b32_e32 v62, v0
	v_mov_b32_e32 v63, v0
	v_mov_b32_e32 v64, v0
	v_mov_b32_e32 v65, v0
	v_mov_b32_e32 v66, v0
	v_mov_b32_e32 v67, v0
	v_mov_b32_e32 v68, v0
	v_mov_b32_e32 v69, v0
	v_mov_b32_e32 v70, v0
	v_mov_b32_e32 v71, v0
	v_mov_b32_e32 v80, v0
	v_mov_b32_e32 v81, v0
	v_mov_b32_e32 v82, v0
	v_mov_b32_e32 v83, v0
	v_mov_b32_e32 v84, v0
	v_mov_b32_e32 v85, v0
	v_mov_b32_e32 v86, v0
	v_mov_b32_e32 v87, v0
	v_mov_b32_e32 v96, v0
	v_mov_b32_e32 v97, v0
	v_mov_b32_e32 v98, v0
	v_mov_b32_e32 v99, v0
	v_mov_b32_e32 v100, v0
	v_mov_b32_e32 v101, v0
	v_mov_b32_e32 v102, v0
	v_mov_b32_e32 v103, v0
	v_mov_b32_e32 v112, v0
	v_mov_b32_e32 v113, v0
	v_mov_b32_e32 v114, v0
	v_mov_b32_e32 v115, v0
	v_mov_b32_e32 v116, v0
	v_mov_b32_e32 v117, v0
	v_mov_b32_e32 v118, v0
	v_mov_b32_e32 v119, v0
	v_mov_b32_e32 v72, v0
	v_mov_b32_e32 v73, v0
	v_mov_b32_e32 v74, v0
	v_mov_b32_e32 v75, v0
	v_mov_b32_e32 v76, v0
	v_mov_b32_e32 v77, v0
	v_mov_b32_e32 v78, v0
	v_mov_b32_e32 v79, v0
	v_mov_b32_e32 v88, v0
	v_mov_b32_e32 v89, v0
	v_mov_b32_e32 v90, v0
	v_mov_b32_e32 v91, v0
	v_mov_b32_e32 v92, v0
	v_mov_b32_e32 v93, v0
	v_mov_b32_e32 v94, v0
	v_mov_b32_e32 v95, v0
	v_mov_b32_e32 v104, v0
	v_mov_b32_e32 v105, v0
	v_mov_b32_e32 v106, v0
	v_mov_b32_e32 v107, v0
	v_mov_b32_e32 v108, v0
	v_mov_b32_e32 v109, v0
	v_mov_b32_e32 v110, v0
	v_mov_b32_e32 v111, v0
	v_mov_b32_e32 v120, v0
	v_mov_b32_e32 v121, v0
	v_mov_b32_e32 v122, v0
	v_mov_b32_e32 v123, v0
	v_mov_b32_e32 v124, v0
	v_mov_b32_e32 v125, v0
	v_mov_b32_e32 v126, v0
	v_mov_b32_e32 v127, v0
	.p2align	6

.LBB0_1221:
	s_andn2_b64 vcc, exec, s[10:11]
	s_cbranch_vccnz .LBB0_1237
	s_add_u32 s68, s44, 0x100
	s_addc_u32 s69, s45, 0
	s_add_u32 s70, s42, 0x100
	s_addc_u32 s71, s43, 0
	s_add_u32 s72, s38, 0x100
	s_addc_u32 s73, s39, 0
	s_add_u32 s74, s40, 0x100
	v_mov_b32_e32 v0, 0
	s_addc_u32 s75, s41, 0
	s_mov_b32 s38, 0
	v_mov_b32_e32 v1, v0
	v_mov_b32_e32 v2, v0
	v_mov_b32_e32 v3, v0
	v_mov_b32_e32 v4, v0
	v_mov_b32_e32 v5, v0
	v_mov_b32_e32 v6, v0
	v_mov_b32_e32 v7, v0
	v_mov_b32_e32 v16, v0
	v_mov_b32_e32 v17, v0
	v_mov_b32_e32 v18, v0
	v_mov_b32_e32 v19, v0
	v_mov_b32_e32 v20, v0
	v_mov_b32_e32 v21, v0
	v_mov_b32_e32 v22, v0
	v_mov_b32_e32 v23, v0
	v_mov_b32_e32 v32, v0
	v_mov_b32_e32 v33, v0
	v_mov_b32_e32 v34, v0
	v_mov_b32_e32 v35, v0
	v_mov_b32_e32 v36, v0
	v_mov_b32_e32 v37, v0
	v_mov_b32_e32 v38, v0
	v_mov_b32_e32 v39, v0
	v_mov_b32_e32 v48, v0
	v_mov_b32_e32 v49, v0
	v_mov_b32_e32 v50, v0
	v_mov_b32_e32 v51, v0
	v_mov_b32_e32 v52, v0
	v_mov_b32_e32 v53, v0
	v_mov_b32_e32 v54, v0
	v_mov_b32_e32 v55, v0
	v_mov_b32_e32 v8, v0
	v_mov_b32_e32 v9, v0
	v_mov_b32_e32 v10, v0
	v_mov_b32_e32 v11, v0
	v_mov_b32_e32 v12, v0
	v_mov_b32_e32 v13, v0
	v_mov_b32_e32 v14, v0
	v_mov_b32_e32 v15, v0
	v_mov_b32_e32 v24, v0
	v_mov_b32_e32 v25, v0
	v_mov_b32_e32 v26, v0
	v_mov_b32_e32 v27, v0
	v_mov_b32_e32 v28, v0
	v_mov_b32_e32 v29, v0
	v_mov_b32_e32 v30, v0
	v_mov_b32_e32 v31, v0
	v_mov_b32_e32 v40, v0
	v_mov_b32_e32 v41, v0
	v_mov_b32_e32 v42, v0
	v_mov_b32_e32 v43, v0
	v_mov_b32_e32 v44, v0
	v_mov_b32_e32 v45, v0
	v_mov_b32_e32 v46, v0
	v_mov_b32_e32 v47, v0
	v_mov_b32_e32 v56, v0
	v_mov_b32_e32 v57, v0
	v_mov_b32_e32 v58, v0
	v_mov_b32_e32 v59, v0
	v_mov_b32_e32 v60, v0
	v_mov_b32_e32 v61, v0
	v_mov_b32_e32 v62, v0
	v_mov_b32_e32 v63, v0
	v_mov_b32_e32 v64, v0
	v_mov_b32_e32 v65, v0
	v_mov_b32_e32 v66, v0
	v_mov_b32_e32 v67, v0
	v_mov_b32_e32 v68, v0
	v_mov_b32_e32 v69, v0
	v_mov_b32_e32 v70, v0
	v_mov_b32_e32 v71, v0
	v_mov_b32_e32 v80, v0
	v_mov_b32_e32 v81, v0
	v_mov_b32_e32 v82, v0
	v_mov_b32_e32 v83, v0
	v_mov_b32_e32 v84, v0
	v_mov_b32_e32 v85, v0
	v_mov_b32_e32 v86, v0
	v_mov_b32_e32 v87, v0
	v_mov_b32_e32 v96, v0
	v_mov_b32_e32 v97, v0
	v_mov_b32_e32 v98, v0
	v_mov_b32_e32 v99, v0
	v_mov_b32_e32 v100, v0
	v_mov_b32_e32 v101, v0
	v_mov_b32_e32 v102, v0
	v_mov_b32_e32 v103, v0
	v_mov_b32_e32 v112, v0
	v_mov_b32_e32 v113, v0
	v_mov_b32_e32 v114, v0
	v_mov_b32_e32 v115, v0
	v_mov_b32_e32 v116, v0
	v_mov_b32_e32 v117, v0
	v_mov_b32_e32 v118, v0
	v_mov_b32_e32 v119, v0
	v_mov_b32_e32 v72, v0
	v_mov_b32_e32 v73, v0
	v_mov_b32_e32 v74, v0
	v_mov_b32_e32 v75, v0
	v_mov_b32_e32 v76, v0
	v_mov_b32_e32 v77, v0
	v_mov_b32_e32 v78, v0
	v_mov_b32_e32 v79, v0
	v_mov_b32_e32 v88, v0
	v_mov_b32_e32 v89, v0
	v_mov_b32_e32 v90, v0
	v_mov_b32_e32 v91, v0
	v_mov_b32_e32 v92, v0
	v_mov_b32_e32 v93, v0
	v_mov_b32_e32 v94, v0
	v_mov_b32_e32 v95, v0
	v_mov_b32_e32 v104, v0
	v_mov_b32_e32 v105, v0
	v_mov_b32_e32 v106, v0
	v_mov_b32_e32 v107, v0
	v_mov_b32_e32 v108, v0
	v_mov_b32_e32 v109, v0
	v_mov_b32_e32 v110, v0
	v_mov_b32_e32 v111, v0
	v_mov_b32_e32 v120, v0
	v_mov_b32_e32 v121, v0
	v_mov_b32_e32 v122, v0
	v_mov_b32_e32 v123, v0
	v_mov_b32_e32 v124, v0
	v_mov_b32_e32 v125, v0
	v_mov_b32_e32 v126, v0
	v_mov_b32_e32 v127, v0
	.p2align	6

.LBB0_1250:
	s_andn2_b64 vcc, exec, s[10:11]
	s_cbranch_vccnz .LBB0_1258
	s_add_u32 s65, s44, 0x100
	s_addc_u32 s66, s45, 0
	s_add_u32 s67, s42, 0x100
	s_addc_u32 s68, s43, 0
	s_add_u32 s69, s38, 0x100
	s_addc_u32 s70, s39, 0
	s_add_u32 s71, s40, 0x100
	v_mov_b32_e32 v0, 0
	s_addc_u32 s72, s41, 0
	s_mov_b32 s38, 0
	v_mov_b32_e32 v1, v0
	v_mov_b32_e32 v2, v0
	v_mov_b32_e32 v3, v0
	v_mov_b32_e32 v4, v0
	v_mov_b32_e32 v5, v0
	v_mov_b32_e32 v6, v0
	v_mov_b32_e32 v7, v0
	v_mov_b32_e32 v16, v0
	v_mov_b32_e32 v17, v0
	v_mov_b32_e32 v18, v0
	v_mov_b32_e32 v19, v0
	v_mov_b32_e32 v20, v0
	v_mov_b32_e32 v21, v0
	v_mov_b32_e32 v22, v0
	v_mov_b32_e32 v23, v0
	v_mov_b32_e32 v32, v0
	v_mov_b32_e32 v33, v0
	v_mov_b32_e32 v34, v0
	v_mov_b32_e32 v35, v0
	v_mov_b32_e32 v36, v0
	v_mov_b32_e32 v37, v0
	v_mov_b32_e32 v38, v0
	v_mov_b32_e32 v39, v0
	v_mov_b32_e32 v48, v0
	v_mov_b32_e32 v49, v0
	v_mov_b32_e32 v50, v0
	v_mov_b32_e32 v51, v0
	v_mov_b32_e32 v52, v0
	v_mov_b32_e32 v53, v0
	v_mov_b32_e32 v54, v0
	v_mov_b32_e32 v55, v0
	v_mov_b32_e32 v8, v0
	v_mov_b32_e32 v9, v0
	v_mov_b32_e32 v10, v0
	v_mov_b32_e32 v11, v0
	v_mov_b32_e32 v12, v0
	v_mov_b32_e32 v13, v0
	v_mov_b32_e32 v14, v0
	v_mov_b32_e32 v15, v0
	v_mov_b32_e32 v24, v0
	v_mov_b32_e32 v25, v0
	v_mov_b32_e32 v26, v0
	v_mov_b32_e32 v27, v0
	v_mov_b32_e32 v28, v0
	v_mov_b32_e32 v29, v0
	v_mov_b32_e32 v30, v0
	v_mov_b32_e32 v31, v0
	v_mov_b32_e32 v40, v0
	v_mov_b32_e32 v41, v0
	v_mov_b32_e32 v42, v0
	v_mov_b32_e32 v43, v0
	v_mov_b32_e32 v44, v0
	v_mov_b32_e32 v45, v0
	v_mov_b32_e32 v46, v0
	v_mov_b32_e32 v47, v0
	v_mov_b32_e32 v56, v0
	v_mov_b32_e32 v57, v0
	v_mov_b32_e32 v58, v0
	v_mov_b32_e32 v59, v0
	v_mov_b32_e32 v64, v0
	v_mov_b32_e32 v65, v0
	v_mov_b32_e32 v66, v0
	v_mov_b32_e32 v67, v0
	v_mov_b32_e32 v60, v0
	v_mov_b32_e32 v61, v0
	v_mov_b32_e32 v62, v0
	v_mov_b32_e32 v63, v0
	v_mov_b32_e32 v68, v0
	v_mov_b32_e32 v69, v0
	v_mov_b32_e32 v70, v0
	v_mov_b32_e32 v71, v0
	v_mov_b32_e32 v80, v0
	v_mov_b32_e32 v81, v0
	v_mov_b32_e32 v82, v0
	v_mov_b32_e32 v83, v0
	v_mov_b32_e32 v84, v0
	v_mov_b32_e32 v85, v0
	v_mov_b32_e32 v86, v0
	v_mov_b32_e32 v87, v0
	v_mov_b32_e32 v96, v0
	v_mov_b32_e32 v97, v0
	v_mov_b32_e32 v98, v0
	v_mov_b32_e32 v99, v0
	v_mov_b32_e32 v100, v0
	v_mov_b32_e32 v101, v0
	v_mov_b32_e32 v102, v0
	v_mov_b32_e32 v103, v0
	v_mov_b32_e32 v112, v0
	v_mov_b32_e32 v113, v0
	v_mov_b32_e32 v114, v0
	v_mov_b32_e32 v115, v0
	v_mov_b32_e32 v116, v0
	v_mov_b32_e32 v117, v0
	v_mov_b32_e32 v118, v0
	v_mov_b32_e32 v119, v0
	v_mov_b32_e32 v72, v0
	v_mov_b32_e32 v73, v0
	v_mov_b32_e32 v74, v0
	v_mov_b32_e32 v75, v0
	v_mov_b32_e32 v76, v0
	v_mov_b32_e32 v77, v0
	v_mov_b32_e32 v78, v0
	v_mov_b32_e32 v79, v0
	v_mov_b32_e32 v88, v0
	v_mov_b32_e32 v89, v0
	v_mov_b32_e32 v90, v0
	v_mov_b32_e32 v91, v0
	v_mov_b32_e32 v92, v0
	v_mov_b32_e32 v93, v0
	v_mov_b32_e32 v94, v0
	v_mov_b32_e32 v95, v0
	v_mov_b32_e32 v104, v0
	v_mov_b32_e32 v105, v0
	v_mov_b32_e32 v106, v0
	v_mov_b32_e32 v107, v0
	v_mov_b32_e32 v108, v0
	v_mov_b32_e32 v109, v0
	v_mov_b32_e32 v110, v0
	v_mov_b32_e32 v111, v0
	v_mov_b32_e32 v120, v0
	v_mov_b32_e32 v121, v0
	v_mov_b32_e32 v122, v0
	v_mov_b32_e32 v123, v0
	v_mov_b32_e32 v124, v0
	v_mov_b32_e32 v125, v0
	v_mov_b32_e32 v126, v0
	v_mov_b32_e32 v127, v0
	.p2align	6

.LBB0_1279:
	s_andn2_b64 vcc, exec, s[16:17]
	s_cbranch_vccnz .LBB0_1287
	s_add_u32 s78, s56, 0x100
	s_addc_u32 s79, s57, 0
	s_add_u32 s80, s54, 0x100
	s_addc_u32 s81, s55, 0
	s_add_u32 s82, s52, 0x100
	s_addc_u32 s83, s53, 0
	s_add_u32 s84, s58, 0x100
	v_mov_b32_e32 v0, 0
	s_addc_u32 s85, s59, 0
	s_mov_b32 s52, 0
	v_mov_b32_e32 v1, v0
	v_mov_b32_e32 v2, v0
	v_mov_b32_e32 v3, v0
	v_mov_b32_e32 v8, v0
	v_mov_b32_e32 v9, v0
	v_mov_b32_e32 v10, v0
	v_mov_b32_e32 v11, v0
	v_mov_b32_e32 v16, v0
	v_mov_b32_e32 v17, v0
	v_mov_b32_e32 v18, v0
	v_mov_b32_e32 v19, v0
	v_mov_b32_e32 v24, v0
	v_mov_b32_e32 v25, v0
	v_mov_b32_e32 v26, v0
	v_mov_b32_e32 v27, v0
	v_mov_b32_e32 v32, v0
	v_mov_b32_e32 v33, v0
	v_mov_b32_e32 v34, v0
	v_mov_b32_e32 v35, v0
	v_mov_b32_e32 v40, v0
	v_mov_b32_e32 v41, v0
	v_mov_b32_e32 v42, v0
	v_mov_b32_e32 v43, v0
	v_mov_b32_e32 v48, v0
	v_mov_b32_e32 v49, v0
	v_mov_b32_e32 v50, v0
	v_mov_b32_e32 v51, v0
	v_mov_b32_e32 v56, v0
	v_mov_b32_e32 v57, v0
	v_mov_b32_e32 v58, v0
	v_mov_b32_e32 v59, v0
	v_mov_b32_e32 v4, v0
	v_mov_b32_e32 v5, v0
	v_mov_b32_e32 v6, v0
	v_mov_b32_e32 v7, v0
	v_mov_b32_e32 v12, v0
	v_mov_b32_e32 v13, v0
	v_mov_b32_e32 v14, v0
	v_mov_b32_e32 v15, v0
	v_mov_b32_e32 v20, v0
	v_mov_b32_e32 v21, v0
	v_mov_b32_e32 v22, v0
	v_mov_b32_e32 v23, v0
	v_mov_b32_e32 v28, v0
	v_mov_b32_e32 v29, v0
	v_mov_b32_e32 v30, v0
	v_mov_b32_e32 v31, v0
	v_mov_b32_e32 v36, v0
	v_mov_b32_e32 v37, v0
	v_mov_b32_e32 v38, v0
	v_mov_b32_e32 v39, v0
	v_mov_b32_e32 v44, v0
	v_mov_b32_e32 v45, v0
	v_mov_b32_e32 v46, v0
	v_mov_b32_e32 v47, v0
	v_mov_b32_e32 v52, v0
	v_mov_b32_e32 v53, v0
	v_mov_b32_e32 v54, v0
	v_mov_b32_e32 v55, v0
	v_mov_b32_e32 v60, v0
	v_mov_b32_e32 v61, v0
	v_mov_b32_e32 v62, v0
	v_mov_b32_e32 v63, v0
	v_mov_b32_e32 v64, v0
	v_mov_b32_e32 v65, v0
	v_mov_b32_e32 v66, v0
	v_mov_b32_e32 v67, v0
	v_mov_b32_e32 v72, v0
	v_mov_b32_e32 v73, v0
	v_mov_b32_e32 v74, v0
	v_mov_b32_e32 v75, v0
	v_mov_b32_e32 v80, v0
	v_mov_b32_e32 v81, v0
	v_mov_b32_e32 v82, v0
	v_mov_b32_e32 v83, v0
	v_mov_b32_e32 v88, v0
	v_mov_b32_e32 v89, v0
	v_mov_b32_e32 v90, v0
	v_mov_b32_e32 v91, v0
	v_mov_b32_e32 v100, v0
	v_mov_b32_e32 v101, v0
	v_mov_b32_e32 v102, v0
	v_mov_b32_e32 v103, v0
	v_mov_b32_e32 v108, v0
	v_mov_b32_e32 v109, v0
	v_mov_b32_e32 v110, v0
	v_mov_b32_e32 v111, v0
	v_mov_b32_e32 v120, v0
	v_mov_b32_e32 v121, v0
	v_mov_b32_e32 v122, v0
	v_mov_b32_e32 v123, v0
	v_mov_b32_e32 v128, v0
	v_mov_b32_e32 v129, v0
	v_mov_b32_e32 v130, v0
	v_mov_b32_e32 v131, v0
	v_mov_b32_e32 v68, v0
	v_mov_b32_e32 v69, v0
	v_mov_b32_e32 v70, v0
	v_mov_b32_e32 v71, v0
	v_mov_b32_e32 v76, v0
	v_mov_b32_e32 v77, v0
	v_mov_b32_e32 v78, v0
	v_mov_b32_e32 v79, v0
	v_mov_b32_e32 v84, v0
	v_mov_b32_e32 v85, v0
	v_mov_b32_e32 v86, v0
	v_mov_b32_e32 v87, v0
	v_mov_b32_e32 v92, v0
	v_mov_b32_e32 v93, v0
	v_mov_b32_e32 v94, v0
	v_mov_b32_e32 v95, v0
	v_mov_b32_e32 v104, v0
	v_mov_b32_e32 v105, v0
	v_mov_b32_e32 v106, v0
	v_mov_b32_e32 v107, v0
	v_mov_b32_e32 v112, v0
	v_mov_b32_e32 v113, v0
	v_mov_b32_e32 v114, v0
	v_mov_b32_e32 v115, v0
	v_mov_b32_e32 v124, v0
	v_mov_b32_e32 v125, v0
	v_mov_b32_e32 v126, v0
	v_mov_b32_e32 v127, v0
	v_mov_b32_e32 v132, v0
	v_mov_b32_e32 v133, v0
	v_mov_b32_e32 v134, v0
	v_mov_b32_e32 v135, v0
	.p2align	6

.LBB0_1432:
	s_andn2_b64 vcc, exec, s[22:23]
	s_cbranch_vccnz .LBB0_1458
	s_add_u32 s78, s50, 0x100
	s_addc_u32 s79, s51, 0
	s_add_u32 s80, s48, 0x100
	s_addc_u32 s81, s49, 0
	s_add_u32 s82, s12, 0x100
	s_addc_u32 s83, s13, 0
	s_add_u32 s84, s52, 0x100
	v_mov_b32_e32 v0, 0
	s_addc_u32 s85, s53, 0
	s_mov_b32 s12, 0
	v_mov_b32_e32 v1, v0
	v_mov_b32_e32 v2, v0
	v_mov_b32_e32 v3, v0
	v_mov_b32_e32 v4, v0
	v_mov_b32_e32 v5, v0
	v_mov_b32_e32 v6, v0
	v_mov_b32_e32 v7, v0
	v_mov_b32_e32 v16, v0
	v_mov_b32_e32 v17, v0
	v_mov_b32_e32 v18, v0
	v_mov_b32_e32 v19, v0
	v_mov_b32_e32 v20, v0
	v_mov_b32_e32 v21, v0
	v_mov_b32_e32 v22, v0
	v_mov_b32_e32 v23, v0
	v_mov_b32_e32 v32, v0
	v_mov_b32_e32 v33, v0
	v_mov_b32_e32 v34, v0
	v_mov_b32_e32 v35, v0
	v_mov_b32_e32 v36, v0
	v_mov_b32_e32 v37, v0
	v_mov_b32_e32 v38, v0
	v_mov_b32_e32 v39, v0
	v_mov_b32_e32 v48, v0
	v_mov_b32_e32 v49, v0
	v_mov_b32_e32 v50, v0
	v_mov_b32_e32 v51, v0
	v_mov_b32_e32 v52, v0
	v_mov_b32_e32 v53, v0
	v_mov_b32_e32 v54, v0
	v_mov_b32_e32 v55, v0
	v_mov_b32_e32 v8, v0
	v_mov_b32_e32 v9, v0
	v_mov_b32_e32 v10, v0
	v_mov_b32_e32 v11, v0
	v_mov_b32_e32 v12, v0
	v_mov_b32_e32 v13, v0
	v_mov_b32_e32 v14, v0
	v_mov_b32_e32 v15, v0
	v_mov_b32_e32 v24, v0
	v_mov_b32_e32 v25, v0
	v_mov_b32_e32 v26, v0
	v_mov_b32_e32 v27, v0
	v_mov_b32_e32 v28, v0
	v_mov_b32_e32 v29, v0
	v_mov_b32_e32 v30, v0
	v_mov_b32_e32 v31, v0
	v_mov_b32_e32 v40, v0
	v_mov_b32_e32 v41, v0
	v_mov_b32_e32 v42, v0
	v_mov_b32_e32 v43, v0
	v_mov_b32_e32 v44, v0
	v_mov_b32_e32 v45, v0
	v_mov_b32_e32 v46, v0
	v_mov_b32_e32 v47, v0
	v_mov_b32_e32 v56, v0
	v_mov_b32_e32 v57, v0
	v_mov_b32_e32 v58, v0
	v_mov_b32_e32 v59, v0
	v_mov_b32_e32 v60, v0
	v_mov_b32_e32 v61, v0
	v_mov_b32_e32 v62, v0
	v_mov_b32_e32 v63, v0
	v_mov_b32_e32 v64, v0
	v_mov_b32_e32 v65, v0
	v_mov_b32_e32 v66, v0
	v_mov_b32_e32 v67, v0
	v_mov_b32_e32 v72, v0
	v_mov_b32_e32 v73, v0
	v_mov_b32_e32 v74, v0
	v_mov_b32_e32 v75, v0
	v_mov_b32_e32 v88, v0
	v_mov_b32_e32 v89, v0
	v_mov_b32_e32 v90, v0
	v_mov_b32_e32 v91, v0
	v_mov_b32_e32 v96, v0
	v_mov_b32_e32 v97, v0
	v_mov_b32_e32 v98, v0
	v_mov_b32_e32 v99, v0
	v_mov_b32_e32 v112, v0
	v_mov_b32_e32 v113, v0
	v_mov_b32_e32 v114, v0
	v_mov_b32_e32 v115, v0
	v_mov_b32_e32 v120, v0
	v_mov_b32_e32 v121, v0
	v_mov_b32_e32 v122, v0
	v_mov_b32_e32 v123, v0
	v_mov_b32_e32 v152, v0
	v_mov_b32_e32 v153, v0
	v_mov_b32_e32 v154, v0
	v_mov_b32_e32 v155, v0
	v_mov_b32_e32 v160, v0
	v_mov_b32_e32 v161, v0
	v_mov_b32_e32 v162, v0
	v_mov_b32_e32 v163, v0
	v_mov_b32_e32 v76, v0
	v_mov_b32_e32 v77, v0
	v_mov_b32_e32 v78, v0
	v_mov_b32_e32 v79, v0
	v_mov_b32_e32 v84, v0
	v_mov_b32_e32 v85, v0
	v_mov_b32_e32 v86, v0
	v_mov_b32_e32 v87, v0
	v_mov_b32_e32 v100, v0
	v_mov_b32_e32 v101, v0
	v_mov_b32_e32 v102, v0
	v_mov_b32_e32 v103, v0
	v_mov_b32_e32 v108, v0
	v_mov_b32_e32 v109, v0
	v_mov_b32_e32 v110, v0
	v_mov_b32_e32 v111, v0
	v_mov_b32_e32 v124, v0
	v_mov_b32_e32 v125, v0
	v_mov_b32_e32 v126, v0
	v_mov_b32_e32 v127, v0
	v_mov_b32_e32 v132, v0
	v_mov_b32_e32 v133, v0
	v_mov_b32_e32 v134, v0
	v_mov_b32_e32 v135, v0
	v_mov_b32_e32 v164, v0
	v_mov_b32_e32 v165, v0
	v_mov_b32_e32 v166, v0
	v_mov_b32_e32 v167, v0
	v_mov_b32_e32 v172, v0
	v_mov_b32_e32 v173, v0
	v_mov_b32_e32 v174, v0
	v_mov_b32_e32 v175, v0
	.p2align	6

.LBB0_1669:
	s_andn2_b64 vcc, exec, s[18:19]
	s_cbranch_vccnz .LBB0_1693
	s_add_u32 s70, s48, 0x100
	s_addc_u32 s71, s49, 0
	s_add_u32 s72, s46, 0x100
	s_addc_u32 s73, s47, 0
	s_add_u32 s74, s44, 0x100
	s_addc_u32 s75, s45, 0
	s_add_u32 s76, s50, 0x100
	v_mov_b32_e32 v0, 0
	s_addc_u32 s77, s51, 0
	s_mov_b32 s44, 0
	s_waitcnt lgkmcnt(0)
	v_mov_b32_e32 v1, v0
	v_mov_b32_e32 v2, v0
	v_mov_b32_e32 v3, v0
	v_mov_b32_e32 v4, v0
	v_mov_b32_e32 v5, v0
	v_mov_b32_e32 v6, v0
	v_mov_b32_e32 v7, v0
	v_mov_b32_e32 v16, v0
	v_mov_b32_e32 v17, v0
	v_mov_b32_e32 v18, v0
	v_mov_b32_e32 v19, v0
	v_mov_b32_e32 v20, v0
	v_mov_b32_e32 v21, v0
	v_mov_b32_e32 v22, v0
	v_mov_b32_e32 v23, v0
	v_mov_b32_e32 v32, v0
	v_mov_b32_e32 v33, v0
	v_mov_b32_e32 v34, v0
	v_mov_b32_e32 v35, v0
	v_mov_b32_e32 v36, v0
	v_mov_b32_e32 v37, v0
	v_mov_b32_e32 v38, v0
	v_mov_b32_e32 v39, v0
	v_mov_b32_e32 v48, v0
	v_mov_b32_e32 v49, v0
	v_mov_b32_e32 v50, v0
	v_mov_b32_e32 v51, v0
	v_mov_b32_e32 v52, v0
	v_mov_b32_e32 v53, v0
	v_mov_b32_e32 v54, v0
	v_mov_b32_e32 v55, v0
	v_mov_b32_e32 v8, v0
	v_mov_b32_e32 v9, v0
	v_mov_b32_e32 v10, v0
	v_mov_b32_e32 v11, v0
	v_mov_b32_e32 v12, v0
	v_mov_b32_e32 v13, v0
	v_mov_b32_e32 v14, v0
	v_mov_b32_e32 v15, v0
	v_mov_b32_e32 v24, v0
	v_mov_b32_e32 v25, v0
	v_mov_b32_e32 v26, v0
	v_mov_b32_e32 v27, v0
	v_mov_b32_e32 v28, v0
	v_mov_b32_e32 v29, v0
	v_mov_b32_e32 v30, v0
	v_mov_b32_e32 v31, v0
	v_mov_b32_e32 v40, v0
	v_mov_b32_e32 v41, v0
	v_mov_b32_e32 v42, v0
	v_mov_b32_e32 v43, v0
	v_mov_b32_e32 v44, v0
	v_mov_b32_e32 v45, v0
	v_mov_b32_e32 v46, v0
	v_mov_b32_e32 v47, v0
	v_mov_b32_e32 v56, v0
	v_mov_b32_e32 v57, v0
	v_mov_b32_e32 v58, v0
	v_mov_b32_e32 v59, v0
	v_mov_b32_e32 v60, v0
	v_mov_b32_e32 v61, v0
	v_mov_b32_e32 v62, v0
	v_mov_b32_e32 v63, v0
	v_mov_b32_e32 v64, v0
	v_mov_b32_e32 v65, v0
	v_mov_b32_e32 v66, v0
	v_mov_b32_e32 v67, v0
	v_mov_b32_e32 v68, v0
	v_mov_b32_e32 v69, v0
	v_mov_b32_e32 v70, v0
	v_mov_b32_e32 v71, v0
	v_mov_b32_e32 v80, v0
	v_mov_b32_e32 v81, v0
	v_mov_b32_e32 v82, v0
	v_mov_b32_e32 v83, v0
	v_mov_b32_e32 v84, v0
	v_mov_b32_e32 v85, v0
	v_mov_b32_e32 v86, v0
	v_mov_b32_e32 v87, v0
	v_mov_b32_e32 v96, v0
	v_mov_b32_e32 v97, v0
	v_mov_b32_e32 v98, v0
	v_mov_b32_e32 v99, v0
	v_mov_b32_e32 v100, v0
	v_mov_b32_e32 v101, v0
	v_mov_b32_e32 v102, v0
	v_mov_b32_e32 v103, v0
	v_mov_b32_e32 v112, v0
	v_mov_b32_e32 v113, v0
	v_mov_b32_e32 v114, v0
	v_mov_b32_e32 v115, v0
	v_mov_b32_e32 v120, v0
	v_mov_b32_e32 v121, v0
	v_mov_b32_e32 v122, v0
	v_mov_b32_e32 v123, v0
	v_mov_b32_e32 v72, v0
	v_mov_b32_e32 v73, v0
	v_mov_b32_e32 v74, v0
	v_mov_b32_e32 v75, v0
	v_mov_b32_e32 v76, v0
	v_mov_b32_e32 v77, v0
	v_mov_b32_e32 v78, v0
	v_mov_b32_e32 v79, v0
	v_mov_b32_e32 v88, v0
	v_mov_b32_e32 v89, v0
	v_mov_b32_e32 v90, v0
	v_mov_b32_e32 v91, v0
	v_mov_b32_e32 v92, v0
	v_mov_b32_e32 v93, v0
	v_mov_b32_e32 v94, v0
	v_mov_b32_e32 v95, v0
	v_mov_b32_e32 v104, v0
	v_mov_b32_e32 v105, v0
	v_mov_b32_e32 v106, v0
	v_mov_b32_e32 v107, v0
	v_mov_b32_e32 v108, v0
	v_mov_b32_e32 v109, v0
	v_mov_b32_e32 v110, v0
	v_mov_b32_e32 v111, v0
	v_mov_b32_e32 v124, v0
	v_mov_b32_e32 v125, v0
	v_mov_b32_e32 v126, v0
	v_mov_b32_e32 v127, v0
	v_mov_b32_e32 v116, v0
	v_mov_b32_e32 v117, v0
	v_mov_b32_e32 v118, v0
	v_mov_b32_e32 v119, v0
	.p2align	6

.Lgx_skip:
	s_xor_b32 s32, s32, 0x400
	v_mbcnt_lo_u32_b32 v255, -1, 0
	v_mbcnt_hi_u32_b32 v255, -1, v255
	v_lshlrev_b32_e32 v255, 2, v255
	v_lshl_add_u32 v255, v164, 13, v255
	s_lshl_b32 s89, s46, 2
	v_add_u32_e32 v255, s89, v255
	s_mov_b32 m0, s32
	s_nop 0
	global_load_lds_dword v255, s[98:99]
	global_load_lds_dword v255, s[98:99] offset:256
	s_add_i32 m0, s32, 0x200
	s_nop 0
	global_load_lds_dword v255, s[100:101]
	global_load_lds_dword v255, s[100:101] offset:256
	v_mov_b32_e32 v33, v32
	v_mov_b32_e32 v34, v32
	v_mov_b32_e32 v35, v32
	v_mov_b32_e32 v56, v32
	v_mov_b32_e32 v57, v32
	v_mov_b32_e32 v58, v32
	v_mov_b32_e32 v59, v32
	v_mov_b32_e32 v48, v32
	v_mov_b32_e32 v49, v32
	v_mov_b32_e32 v50, v32
	v_mov_b32_e32 v51, v32
	v_mov_b32_e32 v40, v32
	v_mov_b32_e32 v41, v32
	v_mov_b32_e32 v42, v32
	v_mov_b32_e32 v43, v32
	v_mov_b32_e32 v64, v32
	v_mov_b32_e32 v65, v32
	v_mov_b32_e32 v66, v32
	v_mov_b32_e32 v67, v32
	v_mov_b32_e32 v72, v32
	v_mov_b32_e32 v73, v32
	v_mov_b32_e32 v74, v32
	v_mov_b32_e32 v75, v32
	v_mov_b32_e32 v80, v32
	v_mov_b32_e32 v81, v32
	v_mov_b32_e32 v82, v32
	v_mov_b32_e32 v83, v32
	v_mov_b32_e32 v88, v32
	v_mov_b32_e32 v89, v32
	v_mov_b32_e32 v90, v32
	v_mov_b32_e32 v91, v32
	v_mov_b32_e32 v36, v32
	v_mov_b32_e32 v37, v32
	v_mov_b32_e32 v38, v32
	v_mov_b32_e32 v39, v32
	v_mov_b32_e32 v60, v32
	v_mov_b32_e32 v61, v32
	v_mov_b32_e32 v62, v32
	v_mov_b32_e32 v63, v32
	v_mov_b32_e32 v52, v32
	v_mov_b32_e32 v53, v32
	v_mov_b32_e32 v54, v32
	v_mov_b32_e32 v55, v32
	v_mov_b32_e32 v44, v32
	v_mov_b32_e32 v45, v32
	v_mov_b32_e32 v46, v32
	v_mov_b32_e32 v47, v32
	v_mov_b32_e32 v68, v32
	v_mov_b32_e32 v69, v32
	v_mov_b32_e32 v70, v32
	v_mov_b32_e32 v71, v32
	v_mov_b32_e32 v76, v32
	v_mov_b32_e32 v77, v32
	v_mov_b32_e32 v78, v32
	v_mov_b32_e32 v79, v32
	v_mov_b32_e32 v84, v32
	v_mov_b32_e32 v85, v32
	v_mov_b32_e32 v86, v32
	v_mov_b32_e32 v87, v32
	v_mov_b32_e32 v92, v32
	v_mov_b32_e32 v93, v32
	v_mov_b32_e32 v94, v32
	v_mov_b32_e32 v95, v32
	v_mov_b32_e32 v96, v32
	v_mov_b32_e32 v97, v32
	v_mov_b32_e32 v98, v32
	v_mov_b32_e32 v99, v32
	v_mov_b32_e32 v104, v32
	v_mov_b32_e32 v105, v32
	v_mov_b32_e32 v106, v32
	v_mov_b32_e32 v107, v32
	v_mov_b32_e32 v112, v32
	v_mov_b32_e32 v113, v32
	v_mov_b32_e32 v114, v32
	v_mov_b32_e32 v115, v32
	v_mov_b32_e32 v120, v32
	v_mov_b32_e32 v121, v32
	v_mov_b32_e32 v122, v32
	v_mov_b32_e32 v123, v32
	v_mov_b32_e32 v128, v32
	v_mov_b32_e32 v129, v32
	v_mov_b32_e32 v130, v32
	v_mov_b32_e32 v131, v32
	v_mov_b32_e32 v136, v32
	v_mov_b32_e32 v137, v32
	v_mov_b32_e32 v138, v32
	v_mov_b32_e32 v139, v32
	v_mov_b32_e32 v144, v32
	v_mov_b32_e32 v145, v32
	v_mov_b32_e32 v146, v32
	v_mov_b32_e32 v147, v32
	v_mov_b32_e32 v152, v32
	v_mov_b32_e32 v153, v32
	v_mov_b32_e32 v154, v32
	v_mov_b32_e32 v155, v32
	v_mov_b32_e32 v100, v32
	v_mov_b32_e32 v101, v32
	v_mov_b32_e32 v102, v32
	v_mov_b32_e32 v103, v32
	v_mov_b32_e32 v108, v32
	v_mov_b32_e32 v109, v32
	v_mov_b32_e32 v110, v32
	v_mov_b32_e32 v111, v32
	v_mov_b32_e32 v116, v32
	v_mov_b32_e32 v117, v32
	v_mov_b32_e32 v118, v32
	v_mov_b32_e32 v119, v32
	v_mov_b32_e32 v124, v32
	v_mov_b32_e32 v125, v32
	v_mov_b32_e32 v126, v32
	v_mov_b32_e32 v127, v32
	v_mov_b32_e32 v132, v32
	v_mov_b32_e32 v133, v32
	v_mov_b32_e32 v134, v32
	v_mov_b32_e32 v135, v32
	v_mov_b32_e32 v140, v32
	v_mov_b32_e32 v141, v32
	v_mov_b32_e32 v142, v32
	v_mov_b32_e32 v143, v32
	v_mov_b32_e32 v148, v32
	v_mov_b32_e32 v149, v32
	v_mov_b32_e32 v150, v32
	v_mov_b32_e32 v151, v32
	v_mov_b32_e32 v156, v32
	v_mov_b32_e32 v157, v32
	v_mov_b32_e32 v158, v32
	v_mov_b32_e32 v159, v32
	s_branch .LBB0_2279
	.p2align	6

.LBB0_2363:
	s_andn2_b64 vcc, exec, s[14:15]
	s_cbranch_vccnz .LBB0_2371
	s_add_u32 s45, s54, 0x100
	s_addc_u32 s47, s55, 0
	s_add_u32 s78, s52, 0x100
	s_addc_u32 s79, s53, 0
	s_add_u32 s80, s48, 0x100
	s_addc_u32 s81, s49, 0
	s_add_u32 s82, s50, 0x100
	v_mov_b32_e32 v24, 0
	s_addc_u32 s83, s51, 0
	s_mov_b32 s48, 0
	v_mov_b32_e32 v25, v24
	v_mov_b32_e32 v26, v24
	v_mov_b32_e32 v27, v24
	v_mov_b32_e32 v48, v24
	v_mov_b32_e32 v49, v24
	v_mov_b32_e32 v50, v24
	v_mov_b32_e32 v51, v24
	v_mov_b32_e32 v36, v24
	v_mov_b32_e32 v37, v24
	v_mov_b32_e32 v38, v24
	v_mov_b32_e32 v39, v24
	v_mov_b32_e32 v52, v24
	v_mov_b32_e32 v53, v24
	v_mov_b32_e32 v54, v24
	v_mov_b32_e32 v55, v24
	v_mov_b32_e32 v32, v24
	v_mov_b32_e32 v33, v24
	v_mov_b32_e32 v34, v24
	v_mov_b32_e32 v35, v24
	v_mov_b32_e32 v64, v24
	v_mov_b32_e32 v65, v24
	v_mov_b32_e32 v66, v24
	v_mov_b32_e32 v67, v24
	v_mov_b32_e32 v56, v24
	v_mov_b32_e32 v57, v24
	v_mov_b32_e32 v58, v24
	v_mov_b32_e32 v59, v24
	v_mov_b32_e32 v68, v24
	v_mov_b32_e32 v69, v24
	v_mov_b32_e32 v70, v24
	v_mov_b32_e32 v71, v24
	v_mov_b32_e32 v60, v24
	v_mov_b32_e32 v61, v24
	v_mov_b32_e32 v62, v24
	v_mov_b32_e32 v63, v24
	v_mov_b32_e32 v112, v24
	v_mov_b32_e32 v113, v24
	v_mov_b32_e32 v114, v24
	v_mov_b32_e32 v115, v24
	v_mov_b32_e32 v92, v24
	v_mov_b32_e32 v93, v24
	v_mov_b32_e32 v94, v24
	v_mov_b32_e32 v95, v24
	v_mov_b32_e32 v116, v24
	v_mov_b32_e32 v117, v24
	v_mov_b32_e32 v118, v24
	v_mov_b32_e32 v119, v24
	v_mov_b32_e32 v84, v24
	v_mov_b32_e32 v85, v24
	v_mov_b32_e32 v86, v24
	v_mov_b32_e32 v87, v24
	v_mov_b32_e32 v120, v24
	v_mov_b32_e32 v121, v24
	v_mov_b32_e32 v122, v24
	v_mov_b32_e32 v123, v24
	v_mov_b32_e32 v104, v24
	v_mov_b32_e32 v105, v24
	v_mov_b32_e32 v106, v24
	v_mov_b32_e32 v107, v24
	v_mov_b32_e32 v128, v24
	v_mov_b32_e32 v129, v24
	v_mov_b32_e32 v130, v24
	v_mov_b32_e32 v131, v24
	v_mov_b32_e32 v28, v24
	v_mov_b32_e32 v29, v24
	v_mov_b32_e32 v30, v24
	v_mov_b32_e32 v31, v24
	v_mov_b32_e32 v76, v24
	v_mov_b32_e32 v77, v24
	v_mov_b32_e32 v78, v24
	v_mov_b32_e32 v79, v24
	v_mov_b32_e32 v100, v24
	v_mov_b32_e32 v101, v24
	v_mov_b32_e32 v102, v24
	v_mov_b32_e32 v103, v24
	v_mov_b32_e32 v96, v24
	v_mov_b32_e32 v97, v24
	v_mov_b32_e32 v98, v24
	v_mov_b32_e32 v99, v24
	v_mov_b32_e32 v40, v24
	v_mov_b32_e32 v41, v24
	v_mov_b32_e32 v42, v24
	v_mov_b32_e32 v43, v24
	v_mov_b32_e32 v108, v24
	v_mov_b32_e32 v109, v24
	v_mov_b32_e32 v110, v24
	v_mov_b32_e32 v111, v24
	v_mov_b32_e32 v88, v24
	v_mov_b32_e32 v89, v24
	v_mov_b32_e32 v90, v24
	v_mov_b32_e32 v91, v24
	v_mov_b32_e32 v44, v24
	v_mov_b32_e32 v45, v24
	v_mov_b32_e32 v46, v24
	v_mov_b32_e32 v47, v24
	v_mov_b32_e32 v124, v24
	v_mov_b32_e32 v125, v24
	v_mov_b32_e32 v126, v24
	v_mov_b32_e32 v127, v24
	v_mov_b32_e32 v132, v24
	v_mov_b32_e32 v133, v24
	v_mov_b32_e32 v134, v24
	v_mov_b32_e32 v135, v24
	v_mov_b32_e32 v80, v24
	v_mov_b32_e32 v81, v24
	v_mov_b32_e32 v82, v24
	v_mov_b32_e32 v83, v24
	v_mov_b32_e32 v140, v24
	v_mov_b32_e32 v141, v24
	v_mov_b32_e32 v142, v24
	v_mov_b32_e32 v143, v24
	v_mov_b32_e32 v136, v24
	v_mov_b32_e32 v137, v24
	v_mov_b32_e32 v138, v24
	v_mov_b32_e32 v139, v24
	v_mov_b32_e32 v144, v24
	v_mov_b32_e32 v145, v24
	v_mov_b32_e32 v146, v24
	v_mov_b32_e32 v147, v24
	v_mov_b32_e32 v72, v24
	v_mov_b32_e32 v73, v24
	v_mov_b32_e32 v74, v24
	v_mov_b32_e32 v75, v24
	v_mov_b32_e32 v148, v24
	v_mov_b32_e32 v149, v24
	v_mov_b32_e32 v150, v24
	v_mov_b32_e32 v151, v24
	.p2align	6
